# weight-fold (fuse_ov) loops in PRE and C2: 18 loads per 4-d group issued together with staged vmcnt waits instead of 4 serialized load/wait rounds
# speedup vs baseline: 1.0055x; 1.0055x over previous
.LBB0_49:
	s_add_u32 s82, s79, s4
	s_addc_u32 s83, s80, s5
	global_load_dwordx4 v[76:79], v[42:43], off offset:-268
	global_load_dwordx4 v[80:83], v[42:43], off offset:-12
	global_load_dwordx4 v[120:123], v3, s[82:83]
	global_load_dwordx4 v[116:119], v3, s[82:83] offset:16
	global_load_dwordx4 v[112:115], v3, s[82:83] offset:32
	global_load_dwordx4 v[108:111], v3, s[82:83] offset:48
	s_add_u32 s82, s44, s4
	s_addc_u32 s83, s45, s5
	global_load_dwordx4 v[130:133], v3, s[82:83]
	global_load_dwordx4 v[134:137], v3, s[82:83] offset:16
	global_load_dwordx4 v[138:141], v3, s[82:83] offset:32
	global_load_dwordx4 v[142:145], v3, s[82:83] offset:48
	s_add_u32 s82, s42, s4
	s_addc_u32 s83, s43, s5
	global_load_dwordx4 v[146:149], v3, s[82:83]
	global_load_dwordx4 v[150:153], v3, s[82:83] offset:16
	global_load_dwordx4 v[154:157], v3, s[82:83] offset:32
	global_load_dwordx4 v[158:161], v3, s[82:83] offset:48
	s_add_u32 s82, s20, s4
	s_addc_u32 s83, s33, s5
	global_load_dwordx4 v[162:165], v3, s[82:83]
	global_load_dwordx4 v[166:169], v3, s[82:83] offset:16
	global_load_dwordx4 v[170:173], v3, s[82:83] offset:32
	global_load_dwordx4 v[174:177], v3, s[82:83] offset:48
	v_lshl_add_u64 v[42:43], v[42:43], 0, 16
	s_add_u32 s4, s4, 0x4000
	s_addc_u32 s5, s5, 0
	s_cmp_lg_u32 s4, 0x40000
	s_waitcnt vmcnt(12)
	v_pk_fma_f32 v[74:75], v[80:81], v[120:121], v[74:75] op_sel_hi:[0,1,1]
	v_pk_fma_f32 v[72:73], v[76:77], v[120:121], v[72:73] op_sel_hi:[0,1,1]
	v_pk_fma_f32 v[70:71], v[80:81], v[122:123], v[70:71] op_sel_hi:[0,1,1]
	v_pk_fma_f32 v[68:69], v[76:77], v[122:123], v[68:69] op_sel_hi:[0,1,1]
	v_pk_fma_f32 v[66:67], v[80:81], v[116:117], v[66:67] op_sel_hi:[0,1,1]
	v_pk_fma_f32 v[64:65], v[76:77], v[116:117], v[64:65] op_sel_hi:[0,1,1]
	v_pk_fma_f32 v[62:63], v[80:81], v[118:119], v[62:63] op_sel_hi:[0,1,1]
	v_pk_fma_f32 v[60:61], v[76:77], v[118:119], v[60:61] op_sel_hi:[0,1,1]
	v_pk_fma_f32 v[58:59], v[80:81], v[112:113], v[58:59] op_sel_hi:[0,1,1]
	v_pk_fma_f32 v[56:57], v[76:77], v[112:113], v[56:57] op_sel_hi:[0,1,1]
	v_pk_fma_f32 v[54:55], v[80:81], v[114:115], v[54:55] op_sel_hi:[0,1,1]
	v_pk_fma_f32 v[52:53], v[76:77], v[114:115], v[52:53] op_sel_hi:[0,1,1]
	v_pk_fma_f32 v[50:51], v[80:81], v[108:109], v[50:51] op_sel_hi:[0,1,1]
	v_pk_fma_f32 v[48:49], v[76:77], v[108:109], v[48:49] op_sel_hi:[0,1,1]
	v_pk_fma_f32 v[46:47], v[80:81], v[110:111], v[46:47] op_sel_hi:[0,1,1]
	v_pk_fma_f32 v[44:45], v[76:77], v[110:111], v[44:45] op_sel_hi:[0,1,1]
	s_waitcnt vmcnt(8)
	v_pk_fma_f32 v[74:75], v[80:81], v[130:131], v[74:75] op_sel:[1,0,0]
	v_pk_fma_f32 v[72:73], v[76:77], v[130:131], v[72:73] op_sel:[1,0,0]
	v_pk_fma_f32 v[70:71], v[80:81], v[132:133], v[70:71] op_sel:[1,0,0]
	v_pk_fma_f32 v[68:69], v[76:77], v[132:133], v[68:69] op_sel:[1,0,0]
	v_pk_fma_f32 v[66:67], v[80:81], v[134:135], v[66:67] op_sel:[1,0,0]
	v_pk_fma_f32 v[64:65], v[76:77], v[134:135], v[64:65] op_sel:[1,0,0]
	v_pk_fma_f32 v[62:63], v[80:81], v[136:137], v[62:63] op_sel:[1,0,0]
	v_pk_fma_f32 v[60:61], v[76:77], v[136:137], v[60:61] op_sel:[1,0,0]
	v_pk_fma_f32 v[58:59], v[80:81], v[138:139], v[58:59] op_sel:[1,0,0]
	v_pk_fma_f32 v[56:57], v[76:77], v[138:139], v[56:57] op_sel:[1,0,0]
	v_pk_fma_f32 v[54:55], v[80:81], v[140:141], v[54:55] op_sel:[1,0,0]
	v_pk_fma_f32 v[52:53], v[76:77], v[140:141], v[52:53] op_sel:[1,0,0]
	v_pk_fma_f32 v[50:51], v[80:81], v[142:143], v[50:51] op_sel:[1,0,0]
	v_pk_fma_f32 v[48:49], v[76:77], v[142:143], v[48:49] op_sel:[1,0,0]
	v_pk_fma_f32 v[46:47], v[80:81], v[144:145], v[46:47] op_sel:[1,0,0]
	v_pk_fma_f32 v[44:45], v[76:77], v[144:145], v[44:45] op_sel:[1,0,0]
	s_waitcnt vmcnt(4)
	v_pk_fma_f32 v[74:75], v[82:83], v[146:147], v[74:75] op_sel_hi:[0,1,1]
	v_pk_fma_f32 v[72:73], v[78:79], v[146:147], v[72:73] op_sel_hi:[0,1,1]
	v_pk_fma_f32 v[70:71], v[82:83], v[148:149], v[70:71] op_sel_hi:[0,1,1]
	v_pk_fma_f32 v[68:69], v[78:79], v[148:149], v[68:69] op_sel_hi:[0,1,1]
	v_pk_fma_f32 v[66:67], v[82:83], v[150:151], v[66:67] op_sel_hi:[0,1,1]
	v_pk_fma_f32 v[64:65], v[78:79], v[150:151], v[64:65] op_sel_hi:[0,1,1]
	v_pk_fma_f32 v[62:63], v[82:83], v[152:153], v[62:63] op_sel_hi:[0,1,1]
	v_pk_fma_f32 v[60:61], v[78:79], v[152:153], v[60:61] op_sel_hi:[0,1,1]
	v_pk_fma_f32 v[58:59], v[82:83], v[154:155], v[58:59] op_sel_hi:[0,1,1]
	v_pk_fma_f32 v[56:57], v[78:79], v[154:155], v[56:57] op_sel_hi:[0,1,1]
	v_pk_fma_f32 v[54:55], v[82:83], v[156:157], v[54:55] op_sel_hi:[0,1,1]
	v_pk_fma_f32 v[52:53], v[78:79], v[156:157], v[52:53] op_sel_hi:[0,1,1]
	v_pk_fma_f32 v[50:51], v[82:83], v[158:159], v[50:51] op_sel_hi:[0,1,1]
	v_pk_fma_f32 v[48:49], v[78:79], v[158:159], v[48:49] op_sel_hi:[0,1,1]
	v_pk_fma_f32 v[46:47], v[82:83], v[160:161], v[46:47] op_sel_hi:[0,1,1]
	v_pk_fma_f32 v[44:45], v[78:79], v[160:161], v[44:45] op_sel_hi:[0,1,1]
	s_waitcnt vmcnt(0)
	v_pk_fma_f32 v[74:75], v[82:83], v[162:163], v[74:75] op_sel:[1,0,0]
	v_pk_fma_f32 v[72:73], v[78:79], v[162:163], v[72:73] op_sel:[1,0,0]
	v_pk_fma_f32 v[70:71], v[82:83], v[164:165], v[70:71] op_sel:[1,0,0]
	v_pk_fma_f32 v[68:69], v[78:79], v[164:165], v[68:69] op_sel:[1,0,0]
	v_pk_fma_f32 v[66:67], v[82:83], v[166:167], v[66:67] op_sel:[1,0,0]
	v_pk_fma_f32 v[64:65], v[78:79], v[166:167], v[64:65] op_sel:[1,0,0]
	v_pk_fma_f32 v[62:63], v[82:83], v[168:169], v[62:63] op_sel:[1,0,0]
	v_pk_fma_f32 v[60:61], v[78:79], v[168:169], v[60:61] op_sel:[1,0,0]
	v_pk_fma_f32 v[58:59], v[82:83], v[170:171], v[58:59] op_sel:[1,0,0]
	v_pk_fma_f32 v[56:57], v[78:79], v[170:171], v[56:57] op_sel:[1,0,0]
	v_pk_fma_f32 v[54:55], v[82:83], v[172:173], v[54:55] op_sel:[1,0,0]
	v_pk_fma_f32 v[52:53], v[78:79], v[172:173], v[52:53] op_sel:[1,0,0]
	v_pk_fma_f32 v[50:51], v[82:83], v[174:175], v[50:51] op_sel:[1,0,0]
	v_pk_fma_f32 v[48:49], v[78:79], v[174:175], v[48:49] op_sel:[1,0,0]
	v_pk_fma_f32 v[46:47], v[82:83], v[176:177], v[46:47] op_sel:[1,0,0]
	v_pk_fma_f32 v[44:45], v[78:79], v[176:177], v[44:45] op_sel:[1,0,0]
	s_cbranch_scc1 .LBB0_49
	s_add_i32 s4, s78, 0xfffff990
	s_lshl_b32 s5, s4, 4
	s_lshl_b32 s4, s4, 2
	v_bfe_u32 v2, v72, 16, 1
	s_and_b32 s5, s5, 0x3f0
	s_and_b32 s20, s4, 0x700
	v_add3_u32 v2, v72, v2, s70
	v_bfe_u32 v33, v74, 16, 1
	v_lshl_add_u64 v[42:43], v[28:29], 0, s[20:21]
	v_lshrrev_b32_e32 v2, 16, v2
	v_add3_u32 v33, v74, v33, s70
	s_mul_i32 s20, s5, 0xc00
	v_and_or_b32 v2, v33, s71, v2
	v_lshl_add_u64 v[42:43], v[42:43], 0, s[20:21]
	global_store_dword v[42:43], v2, off
	v_bfe_u32 v2, v73, 16, 1
	v_add3_u32 v2, v73, v2, s70
	v_bfe_u32 v33, v75, 16, 1
	v_lshrrev_b32_e32 v2, 16, v2
	v_add3_u32 v33, v75, v33, s70
	v_and_or_b32 v2, v33, s71, v2
	global_store_dword v[42:43], v2, off offset:3072
	v_bfe_u32 v2, v68, 16, 1
	v_add3_u32 v2, v68, v2, s70
	v_bfe_u32 v33, v70, 16, 1
	v_lshrrev_b32_e32 v2, 16, v2
	v_add3_u32 v33, v70, v33, s70
	v_add_co_u32_e32 v72, vcc, s72, v42
	v_and_or_b32 v2, v33, s71, v2
	s_nop 0
	v_addc_co_u32_e32 v73, vcc, 0, v43, vcc
	global_store_dword v[72:73], v2, off offset:2048
	v_bfe_u32 v2, v69, 16, 1
	v_add3_u32 v2, v69, v2, s70
	v_bfe_u32 v33, v71, 16, 1
	v_lshrrev_b32_e32 v2, 16, v2
	v_add3_u32 v33, v71, v33, s70
	v_add_co_u32_e32 v68, vcc, s55, v42
	v_and_or_b32 v2, v33, s71, v2
	s_nop 0
	v_addc_co_u32_e32 v69, vcc, 0, v43, vcc
	global_store_dword v[68:69], v2, off offset:1024
	v_bfe_u32 v2, v64, 16, 1
	v_add3_u32 v2, v64, v2, s70
	v_bfe_u32 v33, v66, 16, 1
	v_lshrrev_b32_e32 v2, 16, v2
	v_add3_u32 v33, v66, v33, s70
	v_add_co_u32_e32 v68, vcc, s73, v42
	v_and_or_b32 v2, v33, s71, v2
	s_nop 0
	v_addc_co_u32_e32 v69, vcc, 0, v43, vcc
	global_store_dword v[68:69], v2, off
	v_bfe_u32 v2, v65, 16, 1
	v_add3_u32 v2, v65, v2, s70
	v_bfe_u32 v33, v67, 16, 1
	v_lshrrev_b32_e32 v2, 16, v2
	v_add3_u32 v33, v67, v33, s70
	v_and_or_b32 v2, v33, s71, v2
	global_store_dword v[68:69], v2, off offset:3072
	v_bfe_u32 v2, v60, 16, 1
	v_add3_u32 v2, v60, v2, s70
	v_bfe_u32 v33, v62, 16, 1
	v_lshrrev_b32_e32 v2, 16, v2
	v_add3_u32 v33, v62, v33, s70
	v_add_co_u32_e32 v64, vcc, s56, v42
	v_and_or_b32 v2, v33, s71, v2
	s_nop 0
	v_addc_co_u32_e32 v65, vcc, 0, v43, vcc
	global_store_dword v[64:65], v2, off offset:2048
	v_bfe_u32 v2, v61, 16, 1
	v_add3_u32 v2, v61, v2, s70
	v_bfe_u32 v33, v63, 16, 1
	v_lshrrev_b32_e32 v2, 16, v2
	v_add3_u32 v33, v63, v33, s70
	v_add_co_u32_e32 v60, vcc, s74, v42
	v_and_or_b32 v2, v33, s71, v2
	s_nop 0
	v_addc_co_u32_e32 v61, vcc, 0, v43, vcc
	global_store_dword v[60:61], v2, off offset:1024
	v_bfe_u32 v2, v56, 16, 1
	v_add3_u32 v2, v56, v2, s70
	v_bfe_u32 v33, v58, 16, 1
	v_lshrrev_b32_e32 v2, 16, v2
	v_add3_u32 v33, v58, v33, s70
	v_add_co_u32_e32 v60, vcc, s57, v42
	v_and_or_b32 v2, v33, s71, v2
	s_nop 0
	v_addc_co_u32_e32 v61, vcc, 0, v43, vcc
	global_store_dword v[60:61], v2, off
	v_bfe_u32 v2, v57, 16, 1
	v_add3_u32 v2, v57, v2, s70
	v_bfe_u32 v33, v59, 16, 1
	v_lshrrev_b32_e32 v2, 16, v2
	v_add3_u32 v33, v59, v33, s70
	v_and_or_b32 v2, v33, s71, v2
	global_store_dword v[60:61], v2, off offset:3072
	v_bfe_u32 v2, v52, 16, 1
	v_add3_u32 v2, v52, v2, s70
	v_bfe_u32 v33, v54, 16, 1
	v_lshrrev_b32_e32 v2, 16, v2
	v_add3_u32 v33, v54, v33, s70
	v_add_co_u32_e32 v56, vcc, s75, v42
	v_and_or_b32 v2, v33, s71, v2
	s_nop 0
	v_addc_co_u32_e32 v57, vcc, 0, v43, vcc
	global_store_dword v[56:57], v2, off offset:2048
	v_bfe_u32 v2, v53, 16, 1
	v_add3_u32 v2, v53, v2, s70
	v_bfe_u32 v33, v55, 16, 1
	v_lshrrev_b32_e32 v2, 16, v2
	v_add3_u32 v33, v55, v33, s70
	v_add_co_u32_e32 v52, vcc, s58, v42
	v_and_or_b32 v2, v33, s71, v2
	s_nop 0
	v_addc_co_u32_e32 v53, vcc, 0, v43, vcc
	global_store_dword v[52:53], v2, off offset:1024
	v_bfe_u32 v2, v48, 16, 1
	v_add3_u32 v2, v48, v2, s70
	v_bfe_u32 v33, v50, 16, 1
	v_lshrrev_b32_e32 v2, 16, v2
	v_add3_u32 v33, v50, v33, s70
	v_add_co_u32_e32 v52, vcc, s76, v42
	v_and_or_b32 v2, v33, s71, v2
	s_nop 0
	v_addc_co_u32_e32 v53, vcc, 0, v43, vcc
	global_store_dword v[52:53], v2, off
	v_bfe_u32 v2, v49, 16, 1
	v_add3_u32 v2, v49, v2, s70
	v_bfe_u32 v33, v51, 16, 1
	v_lshrrev_b32_e32 v2, 16, v2
	v_add3_u32 v33, v51, v33, s70
	v_and_or_b32 v2, v33, s71, v2
	global_store_dword v[52:53], v2, off offset:3072
	v_bfe_u32 v2, v44, 16, 1
	v_add3_u32 v2, v44, v2, s70
	v_bfe_u32 v33, v46, 16, 1
	v_lshrrev_b32_e32 v2, 16, v2
	v_add3_u32 v33, v46, v33, s70
	v_add_co_u32_e32 v48, vcc, s59, v42
	v_and_or_b32 v2, v33, s71, v2
	s_nop 0
	v_addc_co_u32_e32 v49, vcc, 0, v43, vcc
	global_store_dword v[48:49], v2, off offset:2048
	v_bfe_u32 v2, v45, 16, 1
	v_add3_u32 v2, v45, v2, s70
	v_bfe_u32 v33, v47, 16, 1
	v_lshrrev_b32_e32 v2, 16, v2
	v_add3_u32 v33, v47, v33, s70
	v_add_co_u32_e32 v42, vcc, 0xb000, v42
	v_and_or_b32 v2, v33, s71, v2
	s_nop 0
	v_addc_co_u32_e32 v43, vcc, 0, v43, vcc
	global_store_dword v[42:43], v2, off offset:1024

.LBB0_1841:
	s_add_u32 s58, s68, s6
	s_addc_u32 s59, s84, s7
	global_load_dwordx4 v[2:5], v[10:11], off offset:-268
	global_load_dwordx4 v[6:9], v[10:11], off offset:-12
	global_load_dwordx4 v[56:59], v1, s[58:59]
	global_load_dwordx4 v[52:55], v1, s[58:59] offset:16
	global_load_dwordx4 v[48:51], v1, s[58:59] offset:32
	global_load_dwordx4 v[44:47], v1, s[58:59] offset:48
	s_add_u32 s58, s52, s6
	s_addc_u32 s59, s53, s7
	global_load_dwordx4 v[150:153], v1, s[58:59]
	global_load_dwordx4 v[154:157], v1, s[58:59] offset:16
	global_load_dwordx4 v[158:161], v1, s[58:59] offset:32
	global_load_dwordx4 v[162:165], v1, s[58:59] offset:48
	s_add_u32 s58, s38, s6
	s_addc_u32 s59, s39, s7
	global_load_dwordx4 v[182:185], v1, s[58:59]
	global_load_dwordx4 v[186:189], v1, s[58:59] offset:16
	global_load_dwordx4 v[190:193], v1, s[58:59] offset:32
	global_load_dwordx4 v[194:197], v1, s[58:59] offset:48
	s_add_u32 s58, s4, s6
	s_addc_u32 s59, s33, s7
	global_load_dwordx4 v[166:169], v1, s[58:59]
	global_load_dwordx4 v[170:173], v1, s[58:59] offset:16
	global_load_dwordx4 v[174:177], v1, s[58:59] offset:32
	global_load_dwordx4 v[216:219], v1, s[58:59] offset:48
	v_lshl_add_u64 v[10:11], v[10:11], 0, 16
	s_add_u32 s6, s6, 0x4000
	s_addc_u32 s7, s7, 0
	s_cmp_lg_u32 s6, 0x40000
	s_waitcnt vmcnt(12)
	v_pk_fma_f32 v[42:43], v[6:7], v[56:57], v[42:43] op_sel_hi:[0,1,1]
	v_pk_fma_f32 v[40:41], v[2:3], v[56:57], v[40:41] op_sel_hi:[0,1,1]
	v_pk_fma_f32 v[38:39], v[6:7], v[58:59], v[38:39] op_sel_hi:[0,1,1]
	v_pk_fma_f32 v[36:37], v[2:3], v[58:59], v[36:37] op_sel_hi:[0,1,1]
	v_pk_fma_f32 v[34:35], v[6:7], v[52:53], v[34:35] op_sel_hi:[0,1,1]
	v_pk_fma_f32 v[32:33], v[2:3], v[52:53], v[32:33] op_sel_hi:[0,1,1]
	v_pk_fma_f32 v[30:31], v[6:7], v[54:55], v[30:31] op_sel_hi:[0,1,1]
	v_pk_fma_f32 v[28:29], v[2:3], v[54:55], v[28:29] op_sel_hi:[0,1,1]
	v_pk_fma_f32 v[26:27], v[6:7], v[48:49], v[26:27] op_sel_hi:[0,1,1]
	v_pk_fma_f32 v[24:25], v[2:3], v[48:49], v[24:25] op_sel_hi:[0,1,1]
	v_pk_fma_f32 v[22:23], v[6:7], v[50:51], v[22:23] op_sel_hi:[0,1,1]
	v_pk_fma_f32 v[20:21], v[2:3], v[50:51], v[20:21] op_sel_hi:[0,1,1]
	v_pk_fma_f32 v[18:19], v[6:7], v[44:45], v[18:19] op_sel_hi:[0,1,1]
	v_pk_fma_f32 v[16:17], v[2:3], v[44:45], v[16:17] op_sel_hi:[0,1,1]
	v_pk_fma_f32 v[14:15], v[6:7], v[46:47], v[14:15] op_sel_hi:[0,1,1]
	v_pk_fma_f32 v[12:13], v[2:3], v[46:47], v[12:13] op_sel_hi:[0,1,1]
	s_waitcnt vmcnt(8)
	v_pk_fma_f32 v[42:43], v[6:7], v[150:151], v[42:43] op_sel:[1,0,0]
	v_pk_fma_f32 v[40:41], v[2:3], v[150:151], v[40:41] op_sel:[1,0,0]
	v_pk_fma_f32 v[38:39], v[6:7], v[152:153], v[38:39] op_sel:[1,0,0]
	v_pk_fma_f32 v[36:37], v[2:3], v[152:153], v[36:37] op_sel:[1,0,0]
	v_pk_fma_f32 v[34:35], v[6:7], v[154:155], v[34:35] op_sel:[1,0,0]
	v_pk_fma_f32 v[32:33], v[2:3], v[154:155], v[32:33] op_sel:[1,0,0]
	v_pk_fma_f32 v[30:31], v[6:7], v[156:157], v[30:31] op_sel:[1,0,0]
	v_pk_fma_f32 v[28:29], v[2:3], v[156:157], v[28:29] op_sel:[1,0,0]
	v_pk_fma_f32 v[26:27], v[6:7], v[158:159], v[26:27] op_sel:[1,0,0]
	v_pk_fma_f32 v[24:25], v[2:3], v[158:159], v[24:25] op_sel:[1,0,0]
	v_pk_fma_f32 v[22:23], v[6:7], v[160:161], v[22:23] op_sel:[1,0,0]
	v_pk_fma_f32 v[20:21], v[2:3], v[160:161], v[20:21] op_sel:[1,0,0]
	v_pk_fma_f32 v[18:19], v[6:7], v[162:163], v[18:19] op_sel:[1,0,0]
	v_pk_fma_f32 v[16:17], v[2:3], v[162:163], v[16:17] op_sel:[1,0,0]
	v_pk_fma_f32 v[14:15], v[6:7], v[164:165], v[14:15] op_sel:[1,0,0]
	v_pk_fma_f32 v[12:13], v[2:3], v[164:165], v[12:13] op_sel:[1,0,0]
	s_waitcnt vmcnt(4)
	v_pk_fma_f32 v[42:43], v[8:9], v[182:183], v[42:43] op_sel_hi:[0,1,1]
	v_pk_fma_f32 v[40:41], v[4:5], v[182:183], v[40:41] op_sel_hi:[0,1,1]
	v_pk_fma_f32 v[38:39], v[8:9], v[184:185], v[38:39] op_sel_hi:[0,1,1]
	v_pk_fma_f32 v[36:37], v[4:5], v[184:185], v[36:37] op_sel_hi:[0,1,1]
	v_pk_fma_f32 v[34:35], v[8:9], v[186:187], v[34:35] op_sel_hi:[0,1,1]
	v_pk_fma_f32 v[32:33], v[4:5], v[186:187], v[32:33] op_sel_hi:[0,1,1]
	v_pk_fma_f32 v[30:31], v[8:9], v[188:189], v[30:31] op_sel_hi:[0,1,1]
	v_pk_fma_f32 v[28:29], v[4:5], v[188:189], v[28:29] op_sel_hi:[0,1,1]
	v_pk_fma_f32 v[26:27], v[8:9], v[190:191], v[26:27] op_sel_hi:[0,1,1]
	v_pk_fma_f32 v[24:25], v[4:5], v[190:191], v[24:25] op_sel_hi:[0,1,1]
	v_pk_fma_f32 v[22:23], v[8:9], v[192:193], v[22:23] op_sel_hi:[0,1,1]
	v_pk_fma_f32 v[20:21], v[4:5], v[192:193], v[20:21] op_sel_hi:[0,1,1]
	v_pk_fma_f32 v[18:19], v[8:9], v[194:195], v[18:19] op_sel_hi:[0,1,1]
	v_pk_fma_f32 v[16:17], v[4:5], v[194:195], v[16:17] op_sel_hi:[0,1,1]
	v_pk_fma_f32 v[14:15], v[8:9], v[196:197], v[14:15] op_sel_hi:[0,1,1]
	v_pk_fma_f32 v[12:13], v[4:5], v[196:197], v[12:13] op_sel_hi:[0,1,1]
	s_waitcnt vmcnt(0)
	v_pk_fma_f32 v[42:43], v[8:9], v[166:167], v[42:43] op_sel:[1,0,0]
	v_pk_fma_f32 v[40:41], v[4:5], v[166:167], v[40:41] op_sel:[1,0,0]
	v_pk_fma_f32 v[38:39], v[8:9], v[168:169], v[38:39] op_sel:[1,0,0]
	v_pk_fma_f32 v[36:37], v[4:5], v[168:169], v[36:37] op_sel:[1,0,0]
	v_pk_fma_f32 v[34:35], v[8:9], v[170:171], v[34:35] op_sel:[1,0,0]
	v_pk_fma_f32 v[32:33], v[4:5], v[170:171], v[32:33] op_sel:[1,0,0]
	v_pk_fma_f32 v[30:31], v[8:9], v[172:173], v[30:31] op_sel:[1,0,0]
	v_pk_fma_f32 v[28:29], v[4:5], v[172:173], v[28:29] op_sel:[1,0,0]
	v_pk_fma_f32 v[26:27], v[8:9], v[174:175], v[26:27] op_sel:[1,0,0]
	v_pk_fma_f32 v[24:25], v[4:5], v[174:175], v[24:25] op_sel:[1,0,0]
	v_pk_fma_f32 v[22:23], v[8:9], v[176:177], v[22:23] op_sel:[1,0,0]
	v_pk_fma_f32 v[20:21], v[4:5], v[176:177], v[20:21] op_sel:[1,0,0]
	v_pk_fma_f32 v[18:19], v[8:9], v[216:217], v[18:19] op_sel:[1,0,0]
	v_pk_fma_f32 v[16:17], v[4:5], v[216:217], v[16:17] op_sel:[1,0,0]
	v_pk_fma_f32 v[14:15], v[8:9], v[218:219], v[14:15] op_sel:[1,0,0]
	v_pk_fma_f32 v[12:13], v[4:5], v[218:219], v[12:13] op_sel:[1,0,0]
	s_cbranch_scc1 .LBB0_1841
	s_add_i32 s4, s85, 0xfffff990
	s_lshl_b32 s6, s4, 4
	s_lshl_b32 s4, s4, 2
	v_bfe_u32 v0, v40, 16, 1
	s_and_b32 s6, s6, 0x3f0
	s_and_b32 s96, s4, 0x700
	v_add3_u32 v0, v40, v0, s55
	v_bfe_u32 v4, v42, 16, 1
	v_lshl_add_u64 v[2:3], v[94:95], 0, s[96:97]
	v_lshrrev_b32_e32 v0, 16, v0
	v_add3_u32 v4, v42, v4, s55
	s_mov_b32 s7, 0xffff0000
	s_mul_i32 s96, s6, 0xc00
	v_and_or_b32 v0, v4, s7, v0
	v_lshl_add_u64 v[2:3], v[2:3], 0, s[96:97]
	global_store_dword v[2:3], v0, off
	v_bfe_u32 v0, v41, 16, 1
	v_add3_u32 v0, v41, v0, s55
	v_bfe_u32 v4, v43, 16, 1
	v_lshrrev_b32_e32 v0, 16, v0
	v_add3_u32 v4, v43, v4, s55
	v_and_or_b32 v0, v4, s7, v0
	global_store_dword v[2:3], v0, off offset:3072
	v_bfe_u32 v0, v36, 16, 1
	v_add3_u32 v0, v36, v0, s55
	v_bfe_u32 v4, v38, 16, 1
	v_lshrrev_b32_e32 v0, 16, v0
	v_add3_u32 v4, v38, v4, s55
	s_movk_i32 s4, 0x1000
	v_and_or_b32 v0, v4, s7, v0
	v_add_co_u32_e32 v4, vcc, s4, v2
	s_movk_i32 s4, 0x2000
	s_nop 0
	v_addc_co_u32_e32 v5, vcc, 0, v3, vcc
	global_store_dword v[4:5], v0, off offset:2048
	v_bfe_u32 v0, v37, 16, 1
	v_add3_u32 v0, v37, v0, s55
	v_bfe_u32 v4, v39, 16, 1
	v_lshrrev_b32_e32 v0, 16, v0
	v_add3_u32 v4, v39, v4, s55
	v_and_or_b32 v0, v4, s7, v0
	v_add_co_u32_e32 v4, vcc, s4, v2
	s_movk_i32 s4, 0x3000
	s_nop 0
	v_addc_co_u32_e32 v5, vcc, 0, v3, vcc
	global_store_dword v[4:5], v0, off offset:1024
	v_bfe_u32 v0, v32, 16, 1
	v_add3_u32 v0, v32, v0, s55
	v_bfe_u32 v4, v34, 16, 1
	v_lshrrev_b32_e32 v0, 16, v0
	v_add3_u32 v4, v34, v4, s55
	v_and_or_b32 v0, v4, s7, v0
	v_add_co_u32_e32 v4, vcc, s4, v2
	v_bfe_u32 v6, v35, 16, 1
	s_nop 0
	v_addc_co_u32_e32 v5, vcc, 0, v3, vcc
	global_store_dword v[4:5], v0, off
	v_bfe_u32 v0, v33, 16, 1
	v_add3_u32 v0, v33, v0, s55
	v_lshrrev_b32_e32 v0, 16, v0
	v_add3_u32 v6, v35, v6, s55
	v_and_or_b32 v0, v6, s7, v0
	global_store_dword v[4:5], v0, off offset:3072
	v_bfe_u32 v0, v28, 16, 1
	v_add3_u32 v0, v28, v0, s55
	v_bfe_u32 v4, v30, 16, 1
	v_lshrrev_b32_e32 v0, 16, v0
	v_add3_u32 v4, v30, v4, s55
	s_movk_i32 s4, 0x4000
	v_and_or_b32 v0, v4, s7, v0
	v_add_co_u32_e32 v4, vcc, s4, v2
	s_movk_i32 s4, 0x5000
	s_nop 0
	v_addc_co_u32_e32 v5, vcc, 0, v3, vcc
	global_store_dword v[4:5], v0, off offset:2048
	v_bfe_u32 v0, v29, 16, 1
	v_add3_u32 v0, v29, v0, s55
	v_bfe_u32 v4, v31, 16, 1
	v_lshrrev_b32_e32 v0, 16, v0
	v_add3_u32 v4, v31, v4, s55
	v_and_or_b32 v0, v4, s7, v0
	v_add_co_u32_e32 v4, vcc, s4, v2
	s_movk_i32 s4, 0x6000
	s_nop 0
	v_addc_co_u32_e32 v5, vcc, 0, v3, vcc
	global_store_dword v[4:5], v0, off offset:1024
	v_bfe_u32 v0, v24, 16, 1
	v_add3_u32 v0, v24, v0, s55
	v_bfe_u32 v4, v26, 16, 1
	v_lshrrev_b32_e32 v0, 16, v0
	v_add3_u32 v4, v26, v4, s55
	v_and_or_b32 v0, v4, s7, v0
	v_add_co_u32_e32 v4, vcc, s4, v2
	v_bfe_u32 v6, v27, 16, 1
	s_nop 0
	v_addc_co_u32_e32 v5, vcc, 0, v3, vcc
	global_store_dword v[4:5], v0, off
	v_bfe_u32 v0, v25, 16, 1
	v_add3_u32 v0, v25, v0, s55
	v_lshrrev_b32_e32 v0, 16, v0
	v_add3_u32 v6, v27, v6, s55
	v_and_or_b32 v0, v6, s7, v0
	global_store_dword v[4:5], v0, off offset:3072
	v_bfe_u32 v0, v20, 16, 1
	v_add3_u32 v0, v20, v0, s55
	v_bfe_u32 v4, v22, 16, 1
	v_lshrrev_b32_e32 v0, 16, v0
	v_add3_u32 v4, v22, v4, s55
	s_movk_i32 s4, 0x7000
	v_and_or_b32 v0, v4, s7, v0
	v_add_co_u32_e32 v4, vcc, s4, v2
	s_mov_b32 s4, 0x8000
	s_nop 0
	v_addc_co_u32_e32 v5, vcc, 0, v3, vcc
	global_store_dword v[4:5], v0, off offset:2048
	v_bfe_u32 v0, v21, 16, 1
	v_add3_u32 v0, v21, v0, s55
	v_bfe_u32 v4, v23, 16, 1
	v_lshrrev_b32_e32 v0, 16, v0
	v_add3_u32 v4, v23, v4, s55
	v_and_or_b32 v0, v4, s7, v0
	v_add_co_u32_e32 v4, vcc, s4, v2
	s_mov_b32 s4, 0x9000
	s_nop 0
	v_addc_co_u32_e32 v5, vcc, 0, v3, vcc
	global_store_dword v[4:5], v0, off offset:1024
	v_bfe_u32 v0, v16, 16, 1
	v_add3_u32 v0, v16, v0, s55
	v_bfe_u32 v4, v18, 16, 1
	v_lshrrev_b32_e32 v0, 16, v0
	v_add3_u32 v4, v18, v4, s55
	v_and_or_b32 v0, v4, s7, v0
	v_add_co_u32_e32 v4, vcc, s4, v2
	v_bfe_u32 v6, v19, 16, 1
	s_nop 0
	v_addc_co_u32_e32 v5, vcc, 0, v3, vcc
	global_store_dword v[4:5], v0, off
	v_bfe_u32 v0, v17, 16, 1
	v_add3_u32 v0, v17, v0, s55
	v_lshrrev_b32_e32 v0, 16, v0
	v_add3_u32 v6, v19, v6, s55
	v_and_or_b32 v0, v6, s7, v0
	global_store_dword v[4:5], v0, off offset:3072
	v_bfe_u32 v0, v12, 16, 1
	v_add3_u32 v0, v12, v0, s55
	v_bfe_u32 v4, v14, 16, 1
	v_lshrrev_b32_e32 v0, 16, v0
	v_add3_u32 v4, v14, v4, s55
	s_mov_b32 s4, 0xa000
	v_and_or_b32 v0, v4, s7, v0
	v_add_co_u32_e32 v4, vcc, s4, v2
	v_readlane_b32 s64, v252, 3
	s_nop 0
	v_addc_co_u32_e32 v5, vcc, 0, v3, vcc
	global_store_dword v[4:5], v0, off offset:2048
	v_bfe_u32 v0, v13, 16, 1
	v_add3_u32 v0, v13, v0, s55
	v_bfe_u32 v4, v15, 16, 1
	v_lshrrev_b32_e32 v0, 16, v0
	v_add3_u32 v4, v15, v4, s55
	v_add_co_u32_e32 v2, vcc, 0xb000, v2
	v_and_or_b32 v0, v4, s7, v0
	s_nop 0
	v_addc_co_u32_e32 v3, vcc, 0, v3, vcc
	v_readlane_b32 s65, v255, 10
	v_readlane_b32 s68, v255, 11
	global_store_dword v[2:3], v0, off offset:1024
